# indexer select (n<=128 variant): paired LDS read, DPP all-reduce for OR/AND instead of 6 bpermute rounds, radix loop on SGPRs; vmcnt(0) before the histogram scan reuses pass-A fragment registers
# speedup vs baseline: 1.0315x; 1.0032x over previous
; #define LAS __attribute__((address_space(3)))
; __device__ __forceinline__ unsigned ix_mono(unsigned raw) { return (raw & 0x80000000u) ? ~raw : (raw | 0x80000000u); }
; __device__ __forceinline__ float ix_h2f(unsigned h) { return (float)__builtin_bit_cast(_Float16, (unsigned short)h); }
; template <bool L2> __device__ __forceinline__ void idx_scan(LAS unsigned* row, bool positive, unsigned need, int lane, unsigned& bin_out, unsigned& need_out) {
;     asm volatile("" : "+v"(lane));
;     unsigned c[16], sum = 0;
; #pragma unroll
;     for (int i = 0; i < 16; ++i) { const int p = 16 * lane + i; const int bin = L2 ? (positive ? 1023 - p : p) : (p < 512 ? 511 - p : p); c[i] = row[bin]; row[bin] = 0u; sum += c[i]; }
;     unsigned incl = sum;
; #pragma unroll
;     for (int o = 1; o < 64; o <<= 1) { const unsigned v = __shfl_up(incl, o); if (lane >= o) incl += v; }
;     const unsigned long long m = __ballot(incl >= need);
;     const int Ls = m ? (int)__builtin_ctzll(m) : 63;
;     unsigned cum = incl - sum, fb = 0u, fn = 1u; bool found = false;
; #pragma unroll
;     for (int i = 0; i < 16; ++i) { const int p = 16 * lane + i; const unsigned bin = (unsigned)(L2 ? (positive ? 1023 - p : p) : (p < 512 ? 511 - p : p));
;         if (!found && cum + c[i] >= need) { found = true; fb = bin; fn = need - cum; } cum += c[i]; }
;     bin_out = (unsigned)__shfl((int)fb, Ls); need_out = (unsigned)__shfl((int)fn, Ls);
; }
; __device__ __forceinline__ void idx_unit(Frame& F, const bf16* QI, const bf16* KI, const float* WI, unsigned* MASK, int b, int j) {
;     ...
;         for (int qq = wave * 4; qq < wave * 4 + 4; ++qq) { unsigned bn, nd; idx_scan<false>(hist + qq * IX_HS, true, 256u, lane, bn, nd);
;             if (lane == 0) {
;                 float tsv, tiv;
;                 if (bn < 512u) { tiv = ix_h2f(bn << 6); tsv = ix_h2f((bn + 1u) << 6); }
;                 else { const unsigned mb = bn - 512u; const float mlo = ix_h2f(mb << 6), mhi = ix_h2f((mb + 1u) << 6);
;                     tsv = (mlo == 0.f) ? 0.f : __uint_as_float(__float_as_uint(-mlo) - 1u); tiv = __uint_as_float(__float_as_uint(-mhi) - 1u); }
;                 st[qq] = bn; st[32 + qq] = nd; st[64 + qq] = __float_as_uint(tsv); st[96 + qq] = __float_as_uint(tiv); st[128 + qq] = ix_mono(__float_as_uint(tiv)); st[160 + qq] = 0u; } }
.LBB0_995:
	v_cmp_eq_u32_e32 vcc, 0, v212
	s_mov_b32 s18, 4
	s_mul_i32 s44, s38, 0x4010
	v_readlane_b32 s45, v252, 33
	s_waitcnt lgkmcnt(0)
	s_barrier
	s_waitcnt vmcnt(0)
	s_mov_b64 s[64:65], exec
	s_mov_b64 exec, -1
	s_movk_i32 s46, 0x1004
	s_movk_i32 s47, 0x100
	v_and_b32_e32 v1, 15, v212
	v_lshrrev_b32_e32 v2, 4, v212
	v_mov_b32_e32 v5, s44
	v_mad_u32_u24 v4, v2, s46, v5
	v_cmp_gt_u32_e64 s[58:59], 8, v1
	v_lshlrev_b32_e32 v6, 8, v1
	v_sub_u32_e32 v7, 0x73c, v6
	s_nop 0
	v_cndmask_b32_e64 v6, v6, v7, s[58:59]
	v_add_u32_e32 v6, v4, v6
	v_mov_b32_e32 v7, 4
	v_cndmask_b32_e64 v7, v7, -4, s[58:59]
	v_xor_b32_e32 v8, 0, v1
	v_mad_i32_i24 v9, v8, v7, v6
	ds_read2_b32 v[146:147], v9 offset1:16
	ds_read2_b32 v[148:149], v9 offset0:32 offset1:48
	v_xor_b32_e32 v8, 1, v1
	v_mad_i32_i24 v10, v8, v7, v6
	ds_read2_b32 v[150:151], v10 offset1:16
	ds_read2_b32 v[152:153], v10 offset0:32 offset1:48
	v_xor_b32_e32 v8, 2, v1
	v_mad_i32_i24 v11, v8, v7, v6
	ds_read2_b32 v[154:155], v11 offset1:16
	ds_read2_b32 v[156:157], v11 offset0:32 offset1:48
	v_xor_b32_e32 v8, 3, v1
	v_mad_i32_i24 v12, v8, v7, v6
	ds_read2_b32 v[158:159], v12 offset1:16
	ds_read2_b32 v[160:161], v12 offset0:32 offset1:48
	v_xor_b32_e32 v8, 4, v1
	v_mad_i32_i24 v13, v8, v7, v6
	ds_read2_b32 v[162:163], v13 offset1:16
	ds_read2_b32 v[164:165], v13 offset0:32 offset1:48
	v_xor_b32_e32 v8, 5, v1
	v_mad_i32_i24 v14, v8, v7, v6
	ds_read2_b32 v[166:167], v14 offset1:16
	ds_read2_b32 v[168:169], v14 offset0:32 offset1:48
	v_xor_b32_e32 v8, 6, v1
	v_mad_i32_i24 v15, v8, v7, v6
	ds_read2_b32 v[170:171], v15 offset1:16
	ds_read2_b32 v[172:173], v15 offset0:32 offset1:48
	v_xor_b32_e32 v8, 7, v1
	v_mad_i32_i24 v16, v8, v7, v6
	ds_read2_b32 v[174:175], v16 offset1:16
	ds_read2_b32 v[176:177], v16 offset0:32 offset1:48
	v_xor_b32_e32 v8, 8, v1
	v_mad_i32_i24 v17, v8, v7, v6
	ds_read2_b32 v[178:179], v17 offset1:16
	ds_read2_b32 v[180:181], v17 offset0:32 offset1:48
	v_xor_b32_e32 v8, 9, v1
	v_mad_i32_i24 v18, v8, v7, v6
	ds_read2_b32 v[182:183], v18 offset1:16
	ds_read2_b32 v[184:185], v18 offset0:32 offset1:48
	v_xor_b32_e32 v8, 10, v1
	v_mad_i32_i24 v19, v8, v7, v6
	ds_read2_b32 v[186:187], v19 offset1:16
	ds_read2_b32 v[188:189], v19 offset0:32 offset1:48
	v_xor_b32_e32 v8, 11, v1
	v_mad_i32_i24 v20, v8, v7, v6
	ds_read2_b32 v[190:191], v20 offset1:16
	ds_read2_b32 v[192:193], v20 offset0:32 offset1:48
	v_xor_b32_e32 v8, 12, v1
	v_mad_i32_i24 v21, v8, v7, v6
	ds_read2_b32 v[40:41], v21 offset1:16
	ds_read2_b32 v[42:43], v21 offset0:32 offset1:48
	v_xor_b32_e32 v8, 13, v1
	v_mad_i32_i24 v22, v8, v7, v6
	ds_read2_b32 v[44:45], v22 offset1:16
	ds_read2_b32 v[46:47], v22 offset0:32 offset1:48
	v_xor_b32_e32 v8, 14, v1
	v_mad_i32_i24 v23, v8, v7, v6
	ds_read2_b32 v[48:49], v23 offset1:16
	ds_read2_b32 v[50:51], v23 offset0:32 offset1:48
	v_xor_b32_e32 v8, 15, v1
	v_mad_i32_i24 v24, v8, v7, v6
	ds_read2_b32 v[52:53], v24 offset1:16
	ds_read2_b32 v[54:55], v24 offset0:32 offset1:48
	s_waitcnt lgkmcnt(0)
	v_add3_u32 v26, v146, v147, v148
	v_add3_u32 v26, v26, v149, v150
	v_add3_u32 v26, v26, v151, v152
	v_add3_u32 v26, v26, v153, v154
	v_add3_u32 v26, v26, v155, v156
	v_add3_u32 v26, v26, v157, v158
	v_add3_u32 v26, v26, v159, v160
	v_add3_u32 v26, v26, v161, v162
	v_add3_u32 v26, v26, v163, v164
	v_add3_u32 v26, v26, v165, v166
	v_add3_u32 v26, v26, v167, v168
	v_add3_u32 v26, v26, v169, v170
	v_add3_u32 v26, v26, v171, v172
	v_add3_u32 v26, v26, v173, v174
	v_add3_u32 v26, v26, v175, v176
	v_add3_u32 v26, v26, v177, v178
	v_add3_u32 v26, v26, v179, v180
	v_add3_u32 v26, v26, v181, v182
	v_add3_u32 v26, v26, v183, v184
	v_add3_u32 v26, v26, v185, v186
	v_add3_u32 v26, v26, v187, v188
	v_add3_u32 v26, v26, v189, v190
	v_add3_u32 v26, v26, v191, v192
	v_add3_u32 v26, v26, v193, v40
	v_add3_u32 v26, v26, v41, v42
	v_add3_u32 v26, v26, v43, v44
	v_add3_u32 v26, v26, v45, v46
	v_add3_u32 v26, v26, v47, v48
	v_add3_u32 v26, v26, v49, v50
	v_add3_u32 v26, v26, v51, v52
	v_add3_u32 v26, v26, v53, v54
	v_add_u32_e32 v26, v26, v55
	v_mov_b32_e32 v27, v26
	s_nop 1
	v_add_u32_dpp v27, v27, v27 row_shr:1 row_mask:0xf bank_mask:0xf bound_ctrl:0
	s_nop 1
	v_add_u32_dpp v27, v27, v27 row_shr:2 row_mask:0xf bank_mask:0xf bound_ctrl:0
	s_nop 1
	v_add_u32_dpp v27, v27, v27 row_shr:4 row_mask:0xf bank_mask:0xf bound_ctrl:0
	s_nop 1
	v_add_u32_dpp v27, v27, v27 row_shr:8 row_mask:0xf bank_mask:0xf bound_ctrl:0
	v_sub_u32_e32 v28, v27, v26
	v_cmp_gt_u32_e64 s[60:61], s47, v28
	v_cmp_le_u32_e64 s[62:63], s47, v27
	s_and_b64 s[60:61], s[60:61], s[62:63]
	v_or_b32_e32 v29, 16, v1
	v_cndmask_b32_e64 v29, 0, v29, s[60:61]
	v_cndmask_b32_e64 v30, 0, v28, s[60:61]
	s_nop 1
	v_or_b32_dpp v29, v29, v29 quad_perm:[1,0,3,2] row_mask:0xf bank_mask:0xf
	v_or_b32_dpp v30, v30, v30 quad_perm:[1,0,3,2] row_mask:0xf bank_mask:0xf
	s_nop 1
	v_or_b32_dpp v29, v29, v29 quad_perm:[2,3,0,1] row_mask:0xf bank_mask:0xf
	v_or_b32_dpp v30, v30, v30 quad_perm:[2,3,0,1] row_mask:0xf bank_mask:0xf
	s_nop 1
	v_or_b32_dpp v29, v29, v29 row_half_mirror row_mask:0xf bank_mask:0xf
	v_or_b32_dpp v30, v30, v30 row_half_mirror row_mask:0xf bank_mask:0xf
	s_nop 1
	v_or_b32_dpp v29, v29, v29 row_mirror row_mask:0xf bank_mask:0xf
	v_or_b32_dpp v30, v30, v30 row_mirror row_mask:0xf bank_mask:0xf
	s_nop 1
	v_and_b32_e32 v31, 15, v29
	v_cmp_gt_u32_e64 s[58:59], 8, v31
	v_lshlrev_b32_e32 v32, 6, v31
	v_lshl_add_u32 v32, v1, 2, v32
	v_sub_u32_e32 v33, 0x1fc, v32
	s_nop 0
	v_cndmask_b32_e64 v33, v32, v33, s[58:59]
	v_lshl_add_u32 v33, v33, 2, v4
	ds_read2_b32 v[34:35], v33 offset1:1
	ds_read2_b32 v[36:37], v33 offset0:2 offset1:3
	s_waitcnt lgkmcnt(0)
; __device__ __forceinline__ unsigned ix_mono(unsigned raw) { return (raw & 0x80000000u) ? ~raw : (raw | 0x80000000u); }
; __device__ __forceinline__ float ix_h2f(unsigned h) { return (float)__builtin_bit_cast(_Float16, (unsigned short)h); }
; template <bool L2> __device__ __forceinline__ void idx_scan(LAS unsigned* row, bool positive, unsigned need, int lane, unsigned& bin_out, unsigned& need_out) {
;     ...
;     unsigned cum = incl - sum, fb = 0u, fn = 1u; bool found = false;
; #pragma unroll
;     for (int i = 0; i < 16; ++i) { const int p = 16 * lane + i; const unsigned bin = (unsigned)(L2 ? (positive ? 1023 - p : p) : (p < 512 ? 511 - p : p));
;         if (!found && cum + c[i] >= need) { found = true; fb = bin; fn = need - cum; } cum += c[i]; }
;     bin_out = (unsigned)__shfl((int)fb, Ls); need_out = (unsigned)__shfl((int)fn, Ls);
; __device__ __forceinline__ void idx_unit(Frame& F, const bf16* QI, const bf16* KI, const float* WI, unsigned* MASK, int b, int j) {
;     ...
;                 if (bn < 512u) { tiv = ix_h2f(bn << 6); tsv = ix_h2f((bn + 1u) << 6); }
;                 else { const unsigned mb = bn - 512u; const float mlo = ix_h2f(mb << 6), mhi = ix_h2f((mb + 1u) << 6);
;                     tsv = (mlo == 0.f) ? 0.f : __uint_as_float(__float_as_uint(-mlo) - 1u); tiv = __uint_as_float(__float_as_uint(-mhi) - 1u); }
;                 st[qq] = bn; st[32 + qq] = nd; st[64 + qq] = __float_as_uint(tsv); st[96 + qq] = __float_as_uint(tiv); st[128 + qq] = ix_mono(__float_as_uint(tiv)); st[160 + qq] = 0u; } }
	v_cndmask_b32_e64 v56, v34, v37, s[58:59]
	v_cndmask_b32_e64 v57, v35, v36, s[58:59]
	v_cndmask_b32_e64 v58, v36, v35, s[58:59]
	v_cndmask_b32_e64 v59, v37, v34, s[58:59]
	v_add3_u32 v60, v56, v57, v58
	v_add_u32_e32 v60, v60, v59
	v_mov_b32_e32 v61, v60
	s_nop 1
	v_add_u32_dpp v61, v61, v61 row_shr:1 row_mask:0xf bank_mask:0xf bound_ctrl:0
	s_nop 1
	v_add_u32_dpp v61, v61, v61 row_shr:2 row_mask:0xf bank_mask:0xf bound_ctrl:0
	s_nop 1
	v_add_u32_dpp v61, v61, v61 row_shr:4 row_mask:0xf bank_mask:0xf bound_ctrl:0
	s_nop 1
	v_add_u32_dpp v61, v61, v61 row_shr:8 row_mask:0xf bank_mask:0xf bound_ctrl:0
	v_sub_u32_e32 v62, v61, v60
	v_add_u32_e32 v62, v62, v30
	v_add_u32_e32 v63, v62, v56
	v_add_u32_e32 v64, v63, v57
	v_add_u32_e32 v65, v64, v58
	v_add_u32_e32 v66, v65, v59
	v_cmp_gt_u32_e64 s[60:61], s47, v62
	v_cmp_le_u32_e64 s[62:63], s47, v66
	s_and_b64 s[60:61], s[60:61], s[62:63]
	v_cmp_le_u32_e64 s[62:63], s47, v65
	v_mov_b32_e32 v67, 3
	s_nop 1
	v_cndmask_b32_e64 v67, v67, 2, s[62:63]
	v_cndmask_b32_e64 v68, v65, v64, s[62:63]
	v_cmp_le_u32_e64 s[62:63], s47, v64
	s_nop 1
	v_cndmask_b32_e64 v67, v67, 1, s[62:63]
	v_cndmask_b32_e64 v68, v68, v63, s[62:63]
	v_cmp_le_u32_e64 s[62:63], s47, v63
	s_nop 1
	v_cndmask_b32_e64 v67, v67, 0, s[62:63]
	v_cndmask_b32_e64 v68, v68, v62, s[62:63]
	v_add_u32_e32 v69, v32, v67
	v_sub_u32_e32 v70, 0x1ff, v69
	s_movk_i32 s53, 0x200
	v_cmp_gt_u32_e64 s[62:63], s53, v69
	s_nop 1
	v_cndmask_b32_e64 v69, v69, v70, s[62:63]
	v_sub_u32_e32 v70, 0x100, v68
	v_bfe_u32 v71, v29, 4, 1
	v_cmp_eq_u32_e64 s[62:63], 0, v71
	v_cmp_eq_u32_e64 s[58:59], 0, v1
	s_and_b64 s[62:63], s[62:63], s[58:59]
	v_cndmask_b32_e64 v69, v69, 0, s[62:63]
	v_cndmask_b32_e64 v70, v70, 1, s[62:63]
	s_or_b64 s[60:61], s[60:61], s[62:63]
	s_mov_b64 exec, s[60:61]
	v_lshlrev_b16_e32 v72, 6, v69
	v_add_u16_e32 v74, 64, v72
	v_add_u16_e32 v75, 0x8040, v72
	v_cvt_f32_f16_e32 v73, v72
	v_cvt_f32_f16_e32 v74, v74
	v_cvt_f32_f16_e64 v75, -v75
	v_add_u32_e32 v76, -1, v73
	v_add_u32_e32 v75, -1, v75
	s_mov_b32 s55, 0x8000
	v_cmp_neq_f16_e64 s[62:63], s55, v72
	s_nop 1
	v_cndmask_b32_e64 v76, 0, v76, s[62:63]
	s_movk_i32 s57, 0x1ff
	v_cmp_lt_u32_e64 s[62:63], s57, v69
	s_nop 1
	v_cndmask_b32_e64 v74, v74, v76, s[62:63]
	v_cndmask_b32_e64 v73, v73, v75, s[62:63]
	v_not_b32_e32 v77, v73
	v_cmp_gt_i32_e64 s[62:63], 0, v73
	s_nop 1
	v_cndmask_b32_e64 v77, -|v73|, v77, s[62:63]
	v_lshl_add_u32 v78, v2, 2, s45
	v_add_u32_e32 v78, 0x20080, v78
	ds_write_b32 v78, v69
	ds_write_b32 v78, v70 offset:128
	ds_write_b32 v78, v74 offset:256
	ds_write_b32 v78, v73 offset:384
	ds_write_b32 v78, v77 offset:512
	ds_write_b32 v78, v3 offset:640
	s_mov_b64 exec, -1
	v_lshl_add_u32 v79, v212, 2, s44
	ds_write2st64_b32 v79, v3, v3 offset0:0 offset1:1
	ds_write2st64_b32 v79, v3, v3 offset0:2 offset1:3
	ds_write2st64_b32 v79, v3, v3 offset0:4 offset1:5
	ds_write2st64_b32 v79, v3, v3 offset0:6 offset1:7
	ds_write2st64_b32 v79, v3, v3 offset0:8 offset1:9
	ds_write2st64_b32 v79, v3, v3 offset0:10 offset1:11
	ds_write2st64_b32 v79, v3, v3 offset0:12 offset1:13
	ds_write2st64_b32 v79, v3, v3 offset0:14 offset1:15
	ds_write2st64_b32 v79, v3, v3 offset0:16 offset1:17
	ds_write2st64_b32 v79, v3, v3 offset0:18 offset1:19
	ds_write2st64_b32 v79, v3, v3 offset0:20 offset1:21
	ds_write2st64_b32 v79, v3, v3 offset0:22 offset1:23
	ds_write2st64_b32 v79, v3, v3 offset0:24 offset1:25
	ds_write2st64_b32 v79, v3, v3 offset0:26 offset1:27
	ds_write2st64_b32 v79, v3, v3 offset0:28 offset1:29
	ds_write2st64_b32 v79, v3, v3 offset0:30 offset1:31
	ds_write2st64_b32 v79, v3, v3 offset0:32 offset1:33
	ds_write2st64_b32 v79, v3, v3 offset0:34 offset1:35
	ds_write2st64_b32 v79, v3, v3 offset0:36 offset1:37
	ds_write2st64_b32 v79, v3, v3 offset0:38 offset1:39
	ds_write2st64_b32 v79, v3, v3 offset0:40 offset1:41
	ds_write2st64_b32 v79, v3, v3 offset0:42 offset1:43
	ds_write2st64_b32 v79, v3, v3 offset0:44 offset1:45
	ds_write2st64_b32 v79, v3, v3 offset0:46 offset1:47
	ds_write2st64_b32 v79, v3, v3 offset0:48 offset1:49
	ds_write2st64_b32 v79, v3, v3 offset0:50 offset1:51
	ds_write2st64_b32 v79, v3, v3 offset0:52 offset1:53
	ds_write2st64_b32 v79, v3, v3 offset0:54 offset1:55
	ds_write2st64_b32 v79, v3, v3 offset0:56 offset1:57
	ds_write2st64_b32 v79, v3, v3 offset0:58 offset1:59
	ds_write2st64_b32 v79, v3, v3 offset0:60 offset1:61
	ds_write2st64_b32 v79, v3, v3 offset0:62 offset1:63
	v_cmp_gt_u32_e64 s[62:63], 4, v212
	s_nop 1
	s_mov_b64 exec, s[62:63]
	ds_write_b32 v79, v3 offset:16384
	s_mov_b64 exec, s[64:65]

; #define LAS __attribute__((address_space(3)))
; template <int NS> __device__ __forceinline__ unsigned idx_select(LAS unsigned* row, unsigned n, unsigned need, int lane) {
;     unsigned v[NS], vor = 0u, vand = 0xffffffffu;
; #pragma unroll
;     for (int s = 0; s < NS; ++s) { const unsigned idx = (unsigned)(s * 64 + lane); const bool ok = idx < n; v[s] = ok ? row[idx] : 0u; vor |= v[s]; vand &= ok ? v[s] : 0xffffffffu; }
; #pragma unroll
;     for (int o = 1; o < 64; o <<= 1) { vor |= (unsigned)__shfl_xor((int)vor, o); vand &= (unsigned)__shfl_xor((int)vand, o); }
;     const unsigned diff = vor ^ vand;
;     if (diff == 0u) return vand;
;     const int top = 31 - __builtin_clz(diff);
;     unsigned T = vand & ~((2u << top) - 1u);
;     ...
; #pragma unroll
;         for (int s = 0; s < NS; ++s) c += (unsigned)__builtin_popcountll(__ballot(v[s] >= cand));
;         if (c >= need) T = cand; }
;     return T;
; }
.LBB0_1190:
	v_lshl_add_u32 v20, v212, 2, s18
	ds_read2st64_b32 v[24:25], v20 offset1:1
	v_cmp_gt_u32_e64 s[4:5], s8, v212
	v_cmp_gt_u32_e64 s[6:7], s8, v1
	s_waitcnt lgkmcnt(0)
	v_cndmask_b32_e64 v19, 0, v24, s[4:5]
	v_cndmask_b32_e64 v2, 0, v25, s[6:7]
	v_cndmask_b32_e64 v20, -1, v24, s[4:5]
	v_cndmask_b32_e64 v21, -1, v25, s[6:7]
	v_or_b32_e32 v22, v2, v19
	v_and_b32_e32 v21, v20, v21
	s_nop 1
	v_or_b32_dpp v22, v22, v22 quad_perm:[1,0,3,2] row_mask:0xf bank_mask:0xf
	v_and_b32_dpp v21, v21, v21 quad_perm:[1,0,3,2] row_mask:0xf bank_mask:0xf
	s_nop 1
	v_or_b32_dpp v22, v22, v22 quad_perm:[2,3,0,1] row_mask:0xf bank_mask:0xf
	v_and_b32_dpp v21, v21, v21 quad_perm:[2,3,0,1] row_mask:0xf bank_mask:0xf
	s_nop 1
	v_or_b32_dpp v22, v22, v22 row_half_mirror row_mask:0xf bank_mask:0xf
	v_and_b32_dpp v21, v21, v21 row_half_mirror row_mask:0xf bank_mask:0xf
	s_nop 1
	v_or_b32_dpp v22, v22, v22 row_mirror row_mask:0xf bank_mask:0xf
	v_and_b32_dpp v21, v21, v21 row_mirror row_mask:0xf bank_mask:0xf
	s_nop 1
	v_readlane_b32 s4, v22, 0
	v_readlane_b32 s5, v22, 16
	v_readlane_b32 s6, v22, 32
	v_readlane_b32 s7, v22, 48
	s_or_b32 s4, s4, s5
	s_or_b32 s6, s6, s7
	s_or_b32 s4, s4, s6
	v_readlane_b32 s5, v21, 0
	v_readlane_b32 s6, v21, 16
	v_readlane_b32 s7, v21, 32
	v_readlane_b32 s18, v21, 48
	s_and_b32 s5, s5, s6
	s_and_b32 s7, s7, s18
	s_and_b32 s5, s5, s7
	s_xor_b32 s6, s4, s5
	s_mov_b32 s4, s5
	s_cmp_eq_u32 s6, 0
	s_cbranch_scc1 .Lsel2_done
	s_flbit_i32_b32 s6, s6
	s_sub_i32 s5, 31, s6
	s_lshl_b32 s6, -2, s5
	s_and_b32 s4, s4, s6
.Lsel2_loop:
	s_lshl_b32 s18, 1, s5
	s_or_b32 s18, s18, s4
	v_cmp_le_u32_e32 vcc, s18, v19
	v_cmp_le_u32_e64 s[6:7], s18, v2
	s_bcnt1_i32_b64 s40, vcc
	s_bcnt1_i32_b64 s6, s[6:7]
	s_add_i32 s40, s40, s6
	s_cmp_lt_u32 s40, s43
	s_cselect_b32 s4, s4, s18
	s_add_i32 s5, s5, -1
	s_cmp_lt_i32 s5, 0
	s_cbranch_scc0 .Lsel2_loop
.Lsel2_done:
	v_mov_b32_e32 v22, s4
	s_mov_b64 s[4:5], exec
